# baseline (speedup 1.0000x reference)
.LBB1_3:
	s_mov_b32 s29, s16
	v_add_u32_e32 v0, s29, v101
	ds_read_b128 v[94:97], v0 offset:16384
	ds_read_b128 v[102:105], v0 offset:17408
	ds_read_b128 v[106:109], v0 offset:18432
	ds_read_b128 v[110:113], v0 offset:19456
	ds_read_b128 v[114:117], v0 offset:32768
	ds_read_b128 v[118:121], v0 offset:33792
	ds_read_b128 v[122:125], v0 offset:34816
	ds_read_b128 v[126:129], v0 offset:35840
	s_lshl_b32 s16, s28, 2
	s_or_b32 s16, s16, s23
	s_lshl_b64 s[30:31], s[16:17], 19
	s_add_u32 s16, s6, s30
	s_addc_u32 s31, s7, s31
	s_lshl_b32 s33, s3, 7
	s_ashr_i32 s35, s33, 31
	s_add_u32 s30, s16, s33
	s_addc_u32 s31, s31, s35
	s_add_u32 s34, s4, s33
	s_addc_u32 s35, s5, s35
	s_add_i32 s16, s19, s27
	s_add_i32 m0, s16, 0x4000
	s_nop 0
	global_load_lds_dwordx4 v84, s[30:31]
	v_add_u32_e32 v0, s29, v91
	ds_read_b128 v[130:133], v0
	ds_read_b128 v[134:137], v0 offset:1024
	ds_read_b128 v[138:141], v0 offset:2048
	s_add_i32 m0, s16, 0x6000
	s_nop 0
	global_load_lds_dwordx4 v88, s[30:31]
	ds_read_b128 v[142:145], v0 offset:3072
	ds_read_b128 v[146:149], v0 offset:4096
	ds_read_b128 v[150:153], v0 offset:5120
	s_mov_b32 m0, s16
	s_nop 0
	global_load_lds_dwordx4 v82, s[34:35]
	ds_read_b128 v[154:157], v0 offset:6144
	ds_read_b128 v[158:161], v0 offset:7168
	s_waitcnt vmcnt(3)
	s_waitcnt lgkmcnt(0)
	s_barrier
	s_setprio 1
	s_waitcnt lgkmcnt(0)
	v_mfma_f32_16x16x32_f16 v[78:81], v[94:97], v[130:133], v[78:81]
	s_add_u32 s30, s30, 0x40000
	s_addc_u32 s31, s31, 0
	s_add_i32 m0, s16, 0x8000
	v_mfma_f32_16x16x32_f16 v[74:77], v[106:109], v[130:133], v[74:77]
	global_load_lds_dwordx4 v84, s[30:31]
	v_mfma_f32_16x16x32_f16 v[66:69], v[94:97], v[138:141], v[66:69]
	s_add_i32 m0, s16, 0xa000
	v_mfma_f32_16x16x32_f16 v[58:61], v[106:109], v[138:141], v[58:61]
	global_load_lds_dwordx4 v88, s[30:31]
	v_mfma_f32_16x16x32_f16 v[78:81], v[102:105], v[134:137], v[78:81]
	s_add_i32 m0, s16, 0x2000
	v_mfma_f32_16x16x32_f16 v[74:77], v[110:113], v[134:137], v[74:77]
	global_load_lds_dwordx4 v86, s[34:35]
	v_mfma_f32_16x16x32_f16 v[66:69], v[102:105], v[142:145], v[66:69]
	v_mfma_f32_16x16x32_f16 v[58:61], v[110:113], v[142:145], v[58:61]
	v_mfma_f32_16x16x32_f16 v[54:57], v[94:97], v[146:149], v[54:57]
	v_mfma_f32_16x16x32_f16 v[46:49], v[106:109], v[146:149], v[46:49]
	v_mfma_f32_16x16x32_f16 v[34:37], v[94:97], v[154:157], v[34:37]
	v_mfma_f32_16x16x32_f16 v[26:29], v[106:109], v[154:157], v[26:29]
	v_mfma_f32_16x16x32_f16 v[54:57], v[102:105], v[150:153], v[54:57]
	v_mfma_f32_16x16x32_f16 v[46:49], v[110:113], v[150:153], v[46:49]
	v_mfma_f32_16x16x32_f16 v[34:37], v[102:105], v[158:161], v[34:37]
	v_mfma_f32_16x16x32_f16 v[26:29], v[110:113], v[158:161], v[26:29]
	v_mfma_f32_16x16x32_f16 v[70:73], v[114:117], v[130:133], v[70:73]
	v_mfma_f32_16x16x32_f16 v[62:65], v[122:125], v[130:133], v[62:65]
	v_mfma_f32_16x16x32_f16 v[50:53], v[114:117], v[138:141], v[50:53]
	v_mfma_f32_16x16x32_f16 v[42:45], v[122:125], v[138:141], v[42:45]
	v_mfma_f32_16x16x32_f16 v[70:73], v[118:121], v[134:137], v[70:73]
	v_mfma_f32_16x16x32_f16 v[62:65], v[126:129], v[134:137], v[62:65]
	v_mfma_f32_16x16x32_f16 v[50:53], v[118:121], v[142:145], v[50:53]
	v_mfma_f32_16x16x32_f16 v[42:45], v[126:129], v[142:145], v[42:45]
	v_mfma_f32_16x16x32_f16 v[38:41], v[114:117], v[146:149], v[38:41]
	v_mfma_f32_16x16x32_f16 v[30:33], v[122:125], v[146:149], v[30:33]
	s_add_i32 s3, s3, 1
	s_bitcmp1_b32 s3, 4
	s_addc_u32 s28, s28, 0
	v_mfma_f32_16x16x32_f16 v[22:25], v[114:117], v[154:157], v[22:25]
	s_and_b32 s3, s3, 15
	v_mfma_f32_16x16x32_f16 v[2:5], v[122:125], v[154:157], v[2:5]
	v_mfma_f32_16x16x32_f16 v[38:41], v[118:121], v[150:153], v[38:41]
	v_mfma_f32_16x16x32_f16 v[30:33], v[126:129], v[150:153], v[30:33]
	s_add_i32 s26, s26, -1
	v_mfma_f32_16x16x32_f16 v[22:25], v[118:121], v[158:161], v[22:25]
	s_mov_b32 s16, s24
	s_mov_b32 s24, s27
	v_mfma_f32_16x16x32_f16 v[2:5], v[126:129], v[158:161], v[2:5]
	s_mov_b32 s27, s29
	s_cmp_lg_u32 s26, 0
	s_setprio 0
	s_barrier
	s_cbranch_scc1 .LBB1_3
	s_lshl_b32 s3, s14, 7
	s_add_i32 s17, s25, s3
	s_ashr_i32 s3, s17, 1
	s_lshr_b32 s14, s17, 5
	s_or_b32 s24, s15, s2
	s_and_b32 s14, s14, 62
	s_and_b32 s27, s3, 0xfffffc00
	v_or_b32_e32 v105, s24, v1
	v_lshlrev_b32_e32 v98, 4, v93
	v_or_b32_e32 v102, 16, v93
	v_or_b32_e32 v103, 32, v93
	v_or_b32_e32 v104, 48, v93
	v_mov_b32_e32 v93, 0
	s_and_b32 s16, s24, 0x340
	v_lshlrev_b32_e32 v95, 6, v105
	s_or_b32 s2, s27, s14
	v_lshlrev_b32_e32 v0, 9, v92
	v_and_b32_e32 v110, 0xc00, v95
	v_mov_b32_e32 v111, v93
	s_or_b32 s14, s2, s16
	v_and_b32_e32 v92, 0x200, v0
	v_lshl_add_u64 v[110:111], s[8:9], 0, v[110:111]
	s_or_b32 s30, s14, 0x80
	s_mov_b32 s3, 0
	v_mov_b32_e32 v99, v93
	v_lshl_add_u64 v[110:111], v[110:111], 0, v[92:93]
	s_mov_b32 s2, 0x3e38aa3b
	v_pk_add_f32 v[72:73], v[12:13], v[72:73]
	v_pk_add_f32 v[70:71], v[10:11], v[70:71]
	v_pk_add_f32 v[64:65], v[8:9], v[64:65]
	v_pk_add_f32 v[62:63], v[6:7], v[62:63]
	s_ashr_i32 s31, s30, 31
	v_lshl_add_u64 v[112:113], v[110:111], 0, v[98:99]
	v_pk_mul_f32 v[72:73], v[72:73], s[2:3] op_sel_hi:[1,0]
	v_pk_mul_f32 v[70:71], v[70:71], s[2:3] op_sel_hi:[1,0]
	v_pk_mul_f32 v[64:65], v[64:65], s[2:3] op_sel_hi:[1,0]
	v_pk_mul_f32 v[62:63], v[62:63], s[2:3] op_sel_hi:[1,0]
	s_lshl_b64 s[30:31], s[30:31], 12
	v_lshlrev_b32_e32 v96, 4, v102
	v_mov_b32_e32 v97, v93
	v_pk_add_f32 v[80:81], v[20:21], v[80:81]
	v_pk_add_f32 v[78:79], v[18:19], v[78:79]
	v_pk_add_f32 v[74:75], v[14:15], v[74:75]
	s_ashr_i32 s15, s14, 31
	v_cvt_pk_f16_f32 v70, v70, v71
	v_cvt_pk_f16_f32 v71, v72, v73
	v_cvt_pk_f16_f32 v72, v62, v63
	v_cvt_pk_f16_f32 v73, v64, v65
	v_lshl_add_u64 v[62:63], v[112:113], 0, s[30:31]
	v_pk_add_f32 v[58:59], v[14:15], v[58:59]
	v_pk_mul_f32 v[80:81], v[80:81], s[2:3] op_sel_hi:[1,0]
	v_pk_mul_f32 v[78:79], v[78:79], s[2:3] op_sel_hi:[1,0]
	v_pk_mul_f32 v[74:75], v[74:75], s[2:3] op_sel_hi:[1,0]
	s_lshl_b64 s[28:29], s[14:15], 12
	global_store_dwordx4 v[62:63], v[70:73], off
	v_pk_add_f32 v[62:63], v[20:21], v[68:69]
	v_pk_add_f32 v[64:65], v[18:19], v[66:67]
	v_lshl_add_u64 v[70:71], v[110:111], 0, v[96:97]
	v_pk_mul_f32 v[58:59], v[58:59], s[2:3] op_sel_hi:[1,0]
	v_pk_add_f32 v[52:53], v[12:13], v[52:53]
	v_pk_add_f32 v[50:51], v[10:11], v[50:51]
	v_pk_add_f32 v[44:45], v[8:9], v[44:45]
	v_pk_add_f32 v[42:43], v[6:7], v[42:43]
	v_lshlrev_b32_e32 v0, 4, v103
	v_cvt_pk_f16_f32 v78, v78, v79
	v_cvt_pk_f16_f32 v79, v80, v81
	v_cvt_pk_f16_f32 v80, v74, v75
	v_lshl_add_u64 v[74:75], v[112:113], 0, s[28:29]
	v_pk_mul_f32 v[66:67], v[62:63], s[2:3] op_sel_hi:[1,0]
	v_pk_mul_f32 v[62:63], v[64:65], s[2:3] op_sel_hi:[1,0]
	v_cvt_pk_f16_f32 v64, v58, v59
	v_lshl_add_u64 v[58:59], v[70:71], 0, s[28:29]
	v_pk_mul_f32 v[52:53], v[52:53], s[2:3] op_sel_hi:[1,0]
	v_pk_mul_f32 v[50:51], v[50:51], s[2:3] op_sel_hi:[1,0]
	v_pk_mul_f32 v[44:45], v[44:45], s[2:3] op_sel_hi:[1,0]
	v_pk_mul_f32 v[42:43], v[42:43], s[2:3] op_sel_hi:[1,0]
	s_or_b32 s28, s14, 1
	s_or_b32 s14, s14, 0x81
	v_and_b32_e32 v106, 0xf0, v0
	v_mov_b32_e32 v107, v93
	v_cvt_pk_f16_f32 v50, v50, v51
	v_cvt_pk_f16_f32 v51, v52, v53
	v_cvt_pk_f16_f32 v52, v42, v43
	v_cvt_pk_f16_f32 v53, v44, v45
	v_lshl_add_u64 v[42:43], v[70:71], 0, s[30:31]
	v_pk_add_f32 v[40:41], v[12:13], v[40:41]
	v_pk_add_f32 v[38:39], v[10:11], v[38:39]
	v_pk_add_f32 v[32:33], v[8:9], v[32:33]
	v_pk_add_f32 v[30:31], v[6:7], v[30:31]
	s_ashr_i32 s15, s14, 31
	v_lshlrev_b32_e32 v94, 4, v104
	global_store_dwordx4 v[42:43], v[50:53], off
	v_pk_mul_f32 v[40:41], v[40:41], s[2:3] op_sel_hi:[1,0]
	v_pk_mul_f32 v[38:39], v[38:39], s[2:3] op_sel_hi:[1,0]
	v_lshl_add_u64 v[50:51], v[110:111], 0, v[106:107]
	v_pk_mul_f32 v[32:33], v[32:33], s[2:3] op_sel_hi:[1,0]
	v_pk_mul_f32 v[30:31], v[30:31], s[2:3] op_sel_hi:[1,0]
	s_lshl_b64 s[14:15], s[14:15], 12
	v_and_b32_e32 v108, 0x1f0, v94
	v_mov_b32_e32 v109, v93
	v_pk_add_f32 v[42:43], v[20:21], v[56:57]
	v_pk_add_f32 v[44:45], v[18:19], v[54:55]
	v_pk_add_f32 v[46:47], v[14:15], v[46:47]
	s_ashr_i32 s29, s28, 31
	v_cvt_pk_f16_f32 v38, v38, v39
	v_cvt_pk_f16_f32 v39, v40, v41
	v_cvt_pk_f16_f32 v40, v30, v31
	v_cvt_pk_f16_f32 v41, v32, v33
	v_lshl_add_u64 v[30:31], v[50:51], 0, s[14:15]
	v_pk_add_f32 v[20:21], v[20:21], v[36:37]
	v_pk_add_f32 v[18:19], v[18:19], v[34:35]
	v_pk_add_f32 v[14:15], v[14:15], v[26:27]
	v_pk_add_f32 v[76:77], v[16:17], v[76:77]
	v_pk_add_f32 v[60:61], v[16:17], v[60:61]
	v_pk_mul_f32 v[52:53], v[42:43], s[2:3] op_sel_hi:[1,0]
	v_pk_mul_f32 v[42:43], v[44:45], s[2:3] op_sel_hi:[1,0]
	v_pk_add_f32 v[44:45], v[16:17], v[48:49]
	s_lshl_b64 s[28:29], s[28:29], 12
	global_store_dwordx4 v[30:31], v[38:41], off
	v_lshl_add_u64 v[30:31], v[110:111], 0, v[108:109]
	v_pk_mul_f32 v[20:21], v[20:21], s[2:3] op_sel_hi:[1,0]
	v_pk_mul_f32 v[18:19], v[18:19], s[2:3] op_sel_hi:[1,0]
	v_pk_add_f32 v[16:17], v[16:17], v[28:29]
	v_pk_mul_f32 v[14:15], v[14:15], s[2:3] op_sel_hi:[1,0]
	v_pk_add_f32 v[12:13], v[12:13], v[24:25]
	v_pk_add_f32 v[10:11], v[10:11], v[22:23]
	v_pk_add_f32 v[4:5], v[8:9], v[4:5]
	v_pk_add_f32 v[2:3], v[6:7], v[2:3]
	v_pk_mul_f32 v[76:77], v[76:77], s[2:3] op_sel_hi:[1,0]
	v_pk_mul_f32 v[60:61], v[60:61], s[2:3] op_sel_hi:[1,0]
	v_pk_mul_f32 v[48:49], v[44:45], s[2:3] op_sel_hi:[1,0]
	v_pk_mul_f32 v[44:45], v[46:47], s[2:3] op_sel_hi:[1,0]
	v_lshl_add_u64 v[46:47], v[50:51], 0, s[28:29]
	v_cvt_pk_f16_f32 v18, v18, v19
	v_cvt_pk_f16_f32 v19, v20, v21
	v_pk_mul_f32 v[16:17], v[16:17], s[2:3] op_sel_hi:[1,0]
	v_cvt_pk_f16_f32 v20, v14, v15
	v_lshl_add_u64 v[14:15], v[30:31], 0, s[28:29]
	v_pk_mul_f32 v[12:13], v[12:13], s[2:3] op_sel_hi:[1,0]
	v_pk_mul_f32 v[10:11], v[10:11], s[2:3] op_sel_hi:[1,0]
	v_pk_mul_f32 v[4:5], v[4:5], s[2:3] op_sel_hi:[1,0]
	v_pk_mul_f32 v[2:3], v[2:3], s[2:3] op_sel_hi:[1,0]
	s_add_u32 s28, s20, s22
	v_cvt_pk_f16_f32 v81, v76, v77
	v_cvt_pk_f16_f32 v62, v62, v63
	v_cvt_pk_f16_f32 v63, v66, v67
	v_cvt_pk_f16_f32 v65, v60, v61
	v_cvt_pk_f16_f32 v42, v42, v43
	v_cvt_pk_f16_f32 v43, v52, v53
	v_cvt_pk_f16_f32 v44, v44, v45
	v_cvt_pk_f16_f32 v45, v48, v49
	v_cvt_pk_f16_f32 v21, v16, v17
	v_cvt_pk_f16_f32 v10, v10, v11
	v_cvt_pk_f16_f32 v11, v12, v13
	v_cvt_pk_f16_f32 v12, v2, v3
	v_cvt_pk_f16_f32 v13, v4, v5
	v_lshl_add_u64 v[2:3], v[30:31], 0, s[14:15]
	s_addc_u32 s29, s21, 0
	v_lshlrev_b32_e32 v92, 2, v1
	global_store_dwordx4 v[74:75], v[78:81], off
	global_store_dwordx4 v[58:59], v[62:65], off
	global_store_dwordx4 v[46:47], v[42:45], off
	global_store_dwordx4 v[14:15], v[18:21], off
	global_store_dwordx4 v[2:3], v[10:13], off
	v_lshl_add_u64 v[2:3], s[28:29], 0, v[92:93]
	s_mov_b64 s[28:29], 0x1000
	v_lshl_add_u64 v[10:11], v[2:3], 0, s[28:29]
	global_load_dwordx4 v[22:25], v[10:11], off
	global_load_dwordx4 v[14:17], v[10:11], off offset:16
	global_load_dwordx4 v[6:9], v[10:11], off offset:512
	global_load_dwordx4 v[2:5], v[10:11], off offset:528
	s_mov_b32 s25, 1
	s_mov_b32 s26, 16
	s_mov_b32 s14, 2
	s_mov_b32 s15, 0x18000
	s_mov_b32 s2, 0xc000
	s_mov_b32 s27, 0
	v_mov_b32_e32 v10, v93
	v_mov_b32_e32 v11, v93
	v_mov_b32_e32 v12, v93
	v_mov_b32_e32 v13, v93
	v_mov_b32_e32 v18, v93
	v_mov_b32_e32 v19, v93
	v_mov_b32_e32 v20, v93
	v_mov_b32_e32 v21, v93
	v_mov_b32_e32 v26, v93
	v_mov_b32_e32 v27, v93
	v_mov_b32_e32 v28, v93
	v_mov_b32_e32 v29, v93
	v_mov_b32_e32 v34, v93
	v_mov_b32_e32 v35, v93
	v_mov_b32_e32 v36, v93
	v_mov_b32_e32 v37, v93
	v_mov_b32_e32 v42, v93
	v_mov_b32_e32 v43, v93
	v_mov_b32_e32 v44, v93
	v_mov_b32_e32 v45, v93
	v_mov_b32_e32 v50, v93
	v_mov_b32_e32 v51, v93
	v_mov_b32_e32 v52, v93
	v_mov_b32_e32 v53, v93
	v_mov_b32_e32 v62, v93
	v_mov_b32_e32 v63, v93
	v_mov_b32_e32 v64, v93
	v_mov_b32_e32 v65, v93
	v_mov_b32_e32 v70, v93
	v_mov_b32_e32 v71, v93
	v_mov_b32_e32 v72, v93
	v_mov_b32_e32 v73, v93
	v_mov_b32_e32 v30, v93
	v_mov_b32_e32 v31, v93
	v_mov_b32_e32 v32, v93
	v_mov_b32_e32 v33, v93
	v_mov_b32_e32 v38, v93
	v_mov_b32_e32 v39, v93
	v_mov_b32_e32 v40, v93
	v_mov_b32_e32 v41, v93
	v_mov_b32_e32 v46, v93
	v_mov_b32_e32 v47, v93
	v_mov_b32_e32 v48, v93
	v_mov_b32_e32 v49, v93
	v_mov_b32_e32 v54, v93
	v_mov_b32_e32 v55, v93
	v_mov_b32_e32 v56, v93
	v_mov_b32_e32 v57, v93
	v_mov_b32_e32 v58, v93
	v_mov_b32_e32 v59, v93
	v_mov_b32_e32 v60, v93
	v_mov_b32_e32 v61, v93
	v_mov_b32_e32 v66, v93
	v_mov_b32_e32 v67, v93
	v_mov_b32_e32 v68, v93
	v_mov_b32_e32 v69, v93
	v_mov_b32_e32 v74, v93
	v_mov_b32_e32 v75, v93
	v_mov_b32_e32 v76, v93
	v_mov_b32_e32 v77, v93
	v_mov_b32_e32 v78, v93
	v_mov_b32_e32 v79, v93
	v_mov_b32_e32 v80, v93
	v_mov_b32_e32 v81, v93
.LBB1_5:
	s_mov_b32 s28, s2
	v_add_u32_e32 v1, s28, v101
	ds_read_b128 v[106:109], v1 offset:16384
	ds_read_b128 v[110:113], v1 offset:17408
	ds_read_b128 v[114:117], v1 offset:18432
	ds_read_b128 v[118:121], v1 offset:19456
	ds_read_b128 v[122:125], v1 offset:32768
	ds_read_b128 v[126:129], v1 offset:33792
	ds_read_b128 v[130:133], v1 offset:34816
	ds_read_b128 v[134:137], v1 offset:35840
	s_lshl_b32 s2, s25, 2
	s_or_b32 s2, s2, s23
	s_lshl_b64 s[30:31], s[2:3], 19
	s_add_u32 s2, s6, s30
	s_addc_u32 s29, s7, s31
	s_lshl_b32 s33, s14, 7
	s_ashr_i32 s35, s33, 31
	s_add_u32 s30, s2, s33
	s_addc_u32 s31, s29, s35
	s_add_u32 s34, s4, s33
	s_addc_u32 s35, s5, s35
	s_add_i32 s2, s19, s27
	s_add_i32 m0, s2, 0x4000
	s_nop 0
	global_load_lds_dwordx4 v84, s[30:31]
	v_add_u32_e32 v1, s28, v91
	ds_read_b128 v[138:141], v1
	ds_read_b128 v[142:145], v1 offset:1024
	ds_read_b128 v[146:149], v1 offset:2048
	s_add_i32 m0, s2, 0x6000
	s_nop 0
	global_load_lds_dwordx4 v88, s[30:31]
	ds_read_b128 v[150:153], v1 offset:3072
	ds_read_b128 v[154:157], v1 offset:4096
	ds_read_b128 v[158:161], v1 offset:5120
	s_mov_b32 m0, s2
	s_nop 0
	global_load_lds_dwordx4 v82, s[34:35]
	ds_read_b128 v[162:165], v1 offset:6144
	ds_read_b128 v[166:169], v1 offset:7168
	s_waitcnt vmcnt(3)
	s_waitcnt lgkmcnt(0)
	s_barrier
	s_setprio 1
	s_waitcnt lgkmcnt(0)
	v_mfma_f32_16x16x32_f16 v[78:81], v[106:109], v[138:141], v[78:81]
	s_add_u32 s30, s30, 0x40000
	s_addc_u32 s31, s31, 0
	s_add_i32 m0, s2, 0x8000
	v_mfma_f32_16x16x32_f16 v[74:77], v[114:117], v[138:141], v[74:77]
	global_load_lds_dwordx4 v84, s[30:31]
	v_mfma_f32_16x16x32_f16 v[66:69], v[106:109], v[146:149], v[66:69]
	s_add_i32 m0, s2, 0xa000
	v_mfma_f32_16x16x32_f16 v[58:61], v[114:117], v[146:149], v[58:61]
	global_load_lds_dwordx4 v88, s[30:31]
	v_mfma_f32_16x16x32_f16 v[78:81], v[110:113], v[142:145], v[78:81]
	s_add_i32 m0, s2, 0x2000
	v_mfma_f32_16x16x32_f16 v[74:77], v[118:121], v[142:145], v[74:77]
	global_load_lds_dwordx4 v86, s[34:35]
	v_mfma_f32_16x16x32_f16 v[66:69], v[110:113], v[150:153], v[66:69]
	v_mfma_f32_16x16x32_f16 v[58:61], v[118:121], v[150:153], v[58:61]
	v_mfma_f32_16x16x32_f16 v[54:57], v[106:109], v[154:157], v[54:57]
	v_mfma_f32_16x16x32_f16 v[46:49], v[114:117], v[154:157], v[46:49]
	v_mfma_f32_16x16x32_f16 v[38:41], v[106:109], v[162:165], v[38:41]
	v_mfma_f32_16x16x32_f16 v[30:33], v[114:117], v[162:165], v[30:33]
	v_mfma_f32_16x16x32_f16 v[54:57], v[110:113], v[158:161], v[54:57]
	v_mfma_f32_16x16x32_f16 v[46:49], v[118:121], v[158:161], v[46:49]
	v_mfma_f32_16x16x32_f16 v[38:41], v[110:113], v[166:169], v[38:41]
	v_mfma_f32_16x16x32_f16 v[30:33], v[118:121], v[166:169], v[30:33]
	v_mfma_f32_16x16x32_f16 v[70:73], v[122:125], v[138:141], v[70:73]
	v_mfma_f32_16x16x32_f16 v[62:65], v[130:133], v[138:141], v[62:65]
	v_mfma_f32_16x16x32_f16 v[50:53], v[122:125], v[146:149], v[50:53]
	v_mfma_f32_16x16x32_f16 v[42:45], v[130:133], v[146:149], v[42:45]
	v_mfma_f32_16x16x32_f16 v[70:73], v[126:129], v[142:145], v[70:73]
	v_mfma_f32_16x16x32_f16 v[62:65], v[134:137], v[142:145], v[62:65]
	v_mfma_f32_16x16x32_f16 v[50:53], v[126:129], v[150:153], v[50:53]
	v_mfma_f32_16x16x32_f16 v[42:45], v[134:137], v[150:153], v[42:45]
	v_mfma_f32_16x16x32_f16 v[34:37], v[122:125], v[154:157], v[34:37]
	v_mfma_f32_16x16x32_f16 v[26:29], v[130:133], v[154:157], v[26:29]
	s_add_i32 s14, s14, 1
	s_bitcmp1_b32 s14, 4
	s_addc_u32 s25, s25, 0
	v_mfma_f32_16x16x32_f16 v[18:21], v[122:125], v[162:165], v[18:21]
	s_and_b32 s14, s14, 15
	v_mfma_f32_16x16x32_f16 v[10:13], v[130:133], v[162:165], v[10:13]
	v_mfma_f32_16x16x32_f16 v[34:37], v[126:129], v[158:161], v[34:37]
	v_mfma_f32_16x16x32_f16 v[26:29], v[134:137], v[158:161], v[26:29]
	s_add_i32 s26, s26, -1
	v_mfma_f32_16x16x32_f16 v[18:21], v[126:129], v[166:169], v[18:21]
	s_mov_b32 s2, s15
	s_mov_b32 s15, s27
	v_mfma_f32_16x16x32_f16 v[10:13], v[134:137], v[166:169], v[10:13]
	s_mov_b32 s27, s28
	s_cmp_lg_u32 s26, 0
	s_setprio 0
	s_barrier
	s_cbranch_scc1 .LBB1_5
	s_ashr_i32 s2, s17, 7
	s_and_b32 s3, s2, -16
	s_or_b32 s2, s3, 2
	s_sub_u32 s14, s10, s8
	s_subb_u32 s11, s11, s9
	s_bfe_u32 s6, s17, 0x50006
	s_add_u32 s14, s8, s14
	s_addc_u32 s15, s9, s11
	s_lshr_b32 s11, s24, 6
	s_or_b32 s17, s11, s3
	s_lshl_b32 s17, s17, 8
	s_lshl_b32 s23, s6, 3
	v_bfe_u32 v93, v105, 3, 3
	v_pk_add_f32 v[80:81], v[24:25], v[80:81]
	v_pk_add_f32 v[78:79], v[22:23], v[78:79]
	v_pk_add_f32 v[74:75], v[14:15], v[74:75]
	s_or_b32 s17, s17, s23
	s_or_b32 s11, s2, s11
	v_cvt_pk_f16_f32 v78, v78, v79
	v_cvt_pk_f16_f32 v79, v80, v81
	v_cvt_pk_f16_f32 v80, v74, v75
	v_or_b32_e32 v74, s17, v93
	s_lshl_b32 s11, s11, 8
	v_ashrrev_i32_e32 v75, 31, v74
	v_pk_add_f32 v[72:73], v[8:9], v[72:73]
	v_pk_add_f32 v[70:71], v[6:7], v[70:71]
	v_pk_add_f32 v[62:63], v[2:3], v[62:63]
	s_or_b32 s11, s11, s23
	v_lshlrev_b64 v[74:75], 10, v[74:75]
	v_cvt_pk_f16_f32 v70, v70, v71
	v_cvt_pk_f16_f32 v71, v72, v73
	v_cvt_pk_f16_f32 v72, v62, v63
	v_or_b32_e32 v62, s11, v93
	v_pk_add_f32 v[76:77], v[16:17], v[76:77]
	v_lshl_add_u64 v[74:75], s[14:15], 0, v[74:75]
	v_ashrrev_i32_e32 v63, 31, v62
	v_cvt_pk_f16_f32 v81, v76, v77
	v_lshl_add_u64 v[76:77], v[74:75], 0, v[98:99]
	v_lshlrev_b64 v[62:63], 10, v[62:63]
	global_store_dwordx4 v[76:77], v[78:81], off
	v_pk_add_f32 v[64:65], v[4:5], v[64:65]
	v_lshl_add_u64 v[76:77], s[14:15], 0, v[62:63]
	v_cvt_pk_f16_f32 v73, v64, v65
	v_lshl_add_u64 v[62:63], v[76:77], 0, v[98:99]
	global_store_dwordx4 v[62:63], v[70:73], off
	v_pk_add_f32 v[64:65], v[24:25], v[68:69]
	v_pk_add_f32 v[62:63], v[22:23], v[66:67]
	v_pk_add_f32 v[60:61], v[16:17], v[60:61]
	v_pk_add_f32 v[58:59], v[14:15], v[58:59]
	v_pk_add_f32 v[52:53], v[8:9], v[52:53]
	v_pk_add_f32 v[50:51], v[6:7], v[50:51]
	v_pk_add_f32 v[44:45], v[4:5], v[44:45]
	v_pk_add_f32 v[42:43], v[2:3], v[42:43]
	v_cvt_pk_f16_f32 v62, v62, v63
	v_cvt_pk_f16_f32 v63, v64, v65
	v_cvt_pk_f16_f32 v64, v58, v59
	v_cvt_pk_f16_f32 v65, v60, v61
	v_lshl_add_u64 v[58:59], v[74:75], 0, v[96:97]
	v_cvt_pk_f16_f32 v50, v50, v51
	v_cvt_pk_f16_f32 v51, v52, v53
	v_cvt_pk_f16_f32 v52, v42, v43
	v_cvt_pk_f16_f32 v53, v44, v45
	v_lshl_add_u64 v[42:43], v[76:77], 0, v[96:97]
	v_mov_b32_e32 v1, 0
	global_store_dwordx4 v[58:59], v[62:65], off
	global_store_dwordx4 v[42:43], v[50:53], off
	v_pk_add_f32 v[44:45], v[24:25], v[56:57]
	v_pk_add_f32 v[42:43], v[22:23], v[54:55]
	v_mov_b32_e32 v95, v1
	v_cvt_pk_f16_f32 v42, v42, v43
	v_cvt_pk_f16_f32 v43, v44, v45
	v_pk_add_f32 v[48:49], v[16:17], v[48:49]
	v_pk_add_f32 v[44:45], v[14:15], v[46:47]
	v_pk_add_f32 v[36:37], v[8:9], v[36:37]
	v_pk_add_f32 v[34:35], v[6:7], v[34:35]
	v_pk_add_f32 v[28:29], v[4:5], v[28:29]
	v_pk_add_f32 v[26:27], v[2:3], v[26:27]
	v_pk_add_f32 v[24:25], v[24:25], v[40:41]
	v_pk_add_f32 v[22:23], v[22:23], v[38:39]
	v_pk_add_f32 v[16:17], v[16:17], v[32:33]
	v_pk_add_f32 v[14:15], v[14:15], v[30:31]
	v_pk_add_f32 v[8:9], v[8:9], v[20:21]
	v_pk_add_f32 v[6:7], v[6:7], v[18:19]
	v_pk_add_f32 v[4:5], v[4:5], v[12:13]
	v_pk_add_f32 v[2:3], v[2:3], v[10:11]
	s_add_u32 s14, s20, s22
	v_cvt_pk_f16_f32 v44, v44, v45
	v_cvt_pk_f16_f32 v45, v48, v49
	v_lshl_add_u64 v[46:47], v[74:75], 0, v[0:1]
	v_cvt_pk_f16_f32 v34, v34, v35
	v_cvt_pk_f16_f32 v35, v36, v37
	v_cvt_pk_f16_f32 v36, v26, v27
	v_cvt_pk_f16_f32 v37, v28, v29
	v_lshl_add_u64 v[26:27], v[76:77], 0, v[0:1]
	v_cvt_pk_f16_f32 v22, v22, v23
	v_cvt_pk_f16_f32 v23, v24, v25
	v_cvt_pk_f16_f32 v24, v14, v15
	v_cvt_pk_f16_f32 v25, v16, v17
	v_lshl_add_u64 v[14:15], v[74:75], 0, v[94:95]
	v_cvt_pk_f16_f32 v6, v6, v7
	v_cvt_pk_f16_f32 v7, v8, v9
	v_cvt_pk_f16_f32 v8, v2, v3
	v_cvt_pk_f16_f32 v9, v4, v5
	v_lshl_add_u64 v[2:3], v[76:77], 0, v[94:95]
	s_addc_u32 s15, s21, 0
	v_mov_b32_e32 v93, v1
	global_store_dwordx4 v[46:47], v[42:45], off
	global_store_dwordx4 v[26:27], v[34:37], off
	global_store_dwordx4 v[14:15], v[22:25], off
	global_store_dwordx4 v[2:3], v[6:9], off
	v_lshl_add_u64 v[2:3], s[14:15], 0, v[92:93]
	s_mov_b64 s[14:15], 0x2000
	v_lshl_add_u64 v[2:3], v[2:3], 0, s[14:15]
	global_load_dwordx4 v[20:23], v[2:3], off
	global_load_dwordx4 v[12:15], v[2:3], off offset:16
	global_load_dwordx4 v[8:11], v[2:3], off offset:512
	global_load_dwordx4 v[4:7], v[2:3], off offset:528
	s_add_u32 s11, s12, 0x400000
	s_mov_b32 s7, 2
	v_and_b32_e32 v106, 56, v105
	s_mov_b32 s10, 0
	s_addc_u32 s12, s13, 0
	s_mov_b32 s14, 0xc000
	s_mov_b32 s17, 0x18000
	s_mov_b32 s13, 16
	v_mov_b32_e32 v0, v1
	v_mov_b32_e32 v2, v1
	v_mov_b32_e32 v3, v1
	v_mov_b32_e32 v16, v1
	v_mov_b32_e32 v17, v1
	v_mov_b32_e32 v18, v1
	v_mov_b32_e32 v19, v1
	v_mov_b32_e32 v24, v1
	v_mov_b32_e32 v25, v1
	v_mov_b32_e32 v26, v1
	v_mov_b32_e32 v27, v1
	v_mov_b32_e32 v32, v1
	v_mov_b32_e32 v33, v1
	v_mov_b32_e32 v34, v1
	v_mov_b32_e32 v35, v1
	v_mov_b32_e32 v40, v1
	v_mov_b32_e32 v41, v1
	v_mov_b32_e32 v42, v1
	v_mov_b32_e32 v43, v1
	v_mov_b32_e32 v48, v1
	v_mov_b32_e32 v49, v1
	v_mov_b32_e32 v50, v1
	v_mov_b32_e32 v51, v1
	v_mov_b32_e32 v60, v1
	v_mov_b32_e32 v61, v1
	v_mov_b32_e32 v62, v1
	v_mov_b32_e32 v63, v1
	v_mov_b32_e32 v68, v1
	v_mov_b32_e32 v69, v1
	v_mov_b32_e32 v70, v1
	v_mov_b32_e32 v71, v1
	v_mov_b32_e32 v28, v1
	v_mov_b32_e32 v29, v1
	v_mov_b32_e32 v30, v1
	v_mov_b32_e32 v31, v1
	v_mov_b32_e32 v36, v1
	v_mov_b32_e32 v37, v1
	v_mov_b32_e32 v38, v1
	v_mov_b32_e32 v39, v1
	v_mov_b32_e32 v44, v1
	v_mov_b32_e32 v45, v1
	v_mov_b32_e32 v46, v1
	v_mov_b32_e32 v47, v1
	v_mov_b32_e32 v52, v1
	v_mov_b32_e32 v53, v1
	v_mov_b32_e32 v54, v1
	v_mov_b32_e32 v55, v1
	v_mov_b32_e32 v56, v1
	v_mov_b32_e32 v57, v1
	v_mov_b32_e32 v58, v1
	v_mov_b32_e32 v59, v1
	v_mov_b32_e32 v64, v1
	v_mov_b32_e32 v65, v1
	v_mov_b32_e32 v66, v1
	v_mov_b32_e32 v67, v1
	v_mov_b32_e32 v72, v1
	v_mov_b32_e32 v73, v1
	v_mov_b32_e32 v74, v1
	v_mov_b32_e32 v75, v1
	v_mov_b32_e32 v76, v1
	v_mov_b32_e32 v77, v1
	v_mov_b32_e32 v78, v1
	v_mov_b32_e32 v79, v1
.LBB1_7:
	s_mov_b32 s15, s17
	v_add_u32_e32 v80, s15, v101
	ds_read_b128 v[92:95], v80 offset:16384
	ds_read_b128 v[96:99], v80 offset:17408
	ds_read_b128 v[108:111], v80 offset:18432
	ds_read_b128 v[112:115], v80 offset:19456
	ds_read_b128 v[116:119], v80 offset:32768
	ds_read_b128 v[120:123], v80 offset:33792
	ds_read_b128 v[124:127], v80 offset:34816
	ds_read_b128 v[128:131], v80 offset:35840
	s_lshl_b32 s17, s7, 7
	s_ashr_i32 s23, s17, 31
	s_add_u32 s20, s11, s17
	s_addc_u32 s21, s12, s23
	s_add_u32 s22, s4, s17
	s_addc_u32 s23, s5, s23
	s_add_i32 s17, s19, s14
	s_add_i32 m0, s17, 0x4000
	s_nop 0
	global_load_lds_dwordx4 v84, s[20:21]
	v_add_u32_e32 v80, s15, v91
	ds_read_b128 v[132:135], v80
	ds_read_b128 v[136:139], v80 offset:1024
	ds_read_b128 v[140:143], v80 offset:2048
	s_add_i32 m0, s17, 0x6000
	s_nop 0
	global_load_lds_dwordx4 v88, s[20:21]
	ds_read_b128 v[144:147], v80 offset:3072
	ds_read_b128 v[148:151], v80 offset:4096
	ds_read_b128 v[152:155], v80 offset:5120
	s_mov_b32 m0, s17
	s_nop 0
	global_load_lds_dwordx4 v82, s[22:23]
	ds_read_b128 v[156:159], v80 offset:6144
	ds_read_b128 v[160:163], v80 offset:7168
	s_waitcnt vmcnt(3)
	s_waitcnt lgkmcnt(0)
	s_barrier
	s_setprio 1
	s_waitcnt lgkmcnt(0)
	v_mfma_f32_16x16x32_f16 v[76:79], v[92:95], v[132:135], v[76:79]
	s_add_u32 s20, s20, 0x40000
	s_addc_u32 s21, s21, 0
	s_add_i32 m0, s17, 0x8000
	v_mfma_f32_16x16x32_f16 v[72:75], v[108:111], v[132:135], v[72:75]
	global_load_lds_dwordx4 v84, s[20:21]
	v_mfma_f32_16x16x32_f16 v[64:67], v[92:95], v[140:143], v[64:67]
	s_add_i32 m0, s17, 0xa000
	v_mfma_f32_16x16x32_f16 v[56:59], v[108:111], v[140:143], v[56:59]
	global_load_lds_dwordx4 v88, s[20:21]
	v_mfma_f32_16x16x32_f16 v[76:79], v[96:99], v[136:139], v[76:79]
	s_add_i32 m0, s17, 0x2000
	v_mfma_f32_16x16x32_f16 v[72:75], v[112:115], v[136:139], v[72:75]
	global_load_lds_dwordx4 v86, s[22:23]
	v_mfma_f32_16x16x32_f16 v[64:67], v[96:99], v[144:147], v[64:67]
	v_mfma_f32_16x16x32_f16 v[56:59], v[112:115], v[144:147], v[56:59]
	v_mfma_f32_16x16x32_f16 v[52:55], v[92:95], v[148:151], v[52:55]
	v_mfma_f32_16x16x32_f16 v[44:47], v[108:111], v[148:151], v[44:47]
	v_mfma_f32_16x16x32_f16 v[36:39], v[92:95], v[156:159], v[36:39]
	v_mfma_f32_16x16x32_f16 v[28:31], v[108:111], v[156:159], v[28:31]
	v_mfma_f32_16x16x32_f16 v[52:55], v[96:99], v[152:155], v[52:55]
	v_mfma_f32_16x16x32_f16 v[44:47], v[112:115], v[152:155], v[44:47]
	v_mfma_f32_16x16x32_f16 v[36:39], v[96:99], v[160:163], v[36:39]
	v_mfma_f32_16x16x32_f16 v[28:31], v[112:115], v[160:163], v[28:31]
	v_mfma_f32_16x16x32_f16 v[68:71], v[116:119], v[132:135], v[68:71]
	v_mfma_f32_16x16x32_f16 v[60:63], v[124:127], v[132:135], v[60:63]
	v_mfma_f32_16x16x32_f16 v[48:51], v[116:119], v[140:143], v[48:51]
	v_mfma_f32_16x16x32_f16 v[40:43], v[124:127], v[140:143], v[40:43]
	v_mfma_f32_16x16x32_f16 v[68:71], v[120:123], v[136:139], v[68:71]
	v_mfma_f32_16x16x32_f16 v[60:63], v[128:131], v[136:139], v[60:63]
	v_mfma_f32_16x16x32_f16 v[48:51], v[120:123], v[144:147], v[48:51]
	v_mfma_f32_16x16x32_f16 v[40:43], v[128:131], v[144:147], v[40:43]
	v_mfma_f32_16x16x32_f16 v[32:35], v[116:119], v[148:151], v[32:35]
	v_mfma_f32_16x16x32_f16 v[24:27], v[124:127], v[148:151], v[24:27]
	s_add_i32 s7, s7, 1
	s_cmp_lg_u32 s7, 16
	v_mfma_f32_16x16x32_f16 v[16:19], v[116:119], v[156:159], v[16:19]
	s_cselect_b32 s7, s7, 0
	v_mfma_f32_16x16x32_f16 v[0:3], v[124:127], v[156:159], v[0:3]
	s_add_i32 s13, s13, -1
	v_mfma_f32_16x16x32_f16 v[32:35], v[120:123], v[152:155], v[32:35]
	s_mov_b32 s17, s10
	v_mfma_f32_16x16x32_f16 v[24:27], v[128:131], v[152:155], v[24:27]
	s_mov_b32 s10, s14
	v_mfma_f32_16x16x32_f16 v[16:19], v[120:123], v[160:163], v[16:19]
	s_mov_b32 s14, s15
	v_mfma_f32_16x16x32_f16 v[0:3], v[128:131], v[160:163], v[0:3]
	s_cmp_lg_u32 s13, 0
	s_setprio 0
	s_barrier
	s_cbranch_scc1 .LBB1_7
	s_sub_u32 s0, s0, s8
	s_subb_u32 s1, s1, s9
	s_add_u32 s0, s8, s0
	s_addc_u32 s1, s9, s1
	s_lshl_b32 s3, s3, 6
	s_or_b32 s3, s3, s16
	s_lshl_b32 s4, s6, 1
	v_lshrrev_b32_e32 v86, 5, v106
	v_pk_add_f32 v[78:79], v[22:23], v[78:79]
	v_pk_add_f32 v[76:77], v[20:21], v[76:77]
	v_pk_add_f32 v[72:73], v[12:13], v[72:73]
	s_or_b32 s3, s3, s4
	s_lshl_b32 s2, s2, 6
	v_cvt_pk_f16_f32 v76, v76, v77
	v_cvt_pk_f16_f32 v77, v78, v79
	v_cvt_pk_f16_f32 v78, v72, v73
	v_or_b32_e32 v72, s3, v86
	s_or_b32 s2, s2, s16
	v_ashrrev_i32_e32 v73, 31, v72
	v_pk_add_f32 v[70:71], v[10:11], v[70:71]
	v_pk_add_f32 v[68:69], v[8:9], v[68:69]
	v_pk_add_f32 v[60:61], v[4:5], v[60:61]
	s_or_b32 s2, s2, s4
	v_lshlrev_b64 v[72:73], 12, v[72:73]
	v_cvt_pk_f16_f32 v68, v68, v69
	v_cvt_pk_f16_f32 v69, v70, v71
	v_cvt_pk_f16_f32 v70, v60, v61
	v_or_b32_e32 v60, s2, v86
	v_mov_b32_e32 v91, 0
	v_pk_add_f32 v[74:75], v[14:15], v[74:75]
	v_lshl_add_u64 v[72:73], s[0:1], 0, v[72:73]
	v_ashrrev_i32_e32 v61, 31, v60
	v_cvt_pk_f16_f32 v79, v74, v75
	v_lshl_add_u64 v[74:75], v[72:73], 0, v[90:91]
	v_lshlrev_b64 v[60:61], 12, v[60:61]
	v_lshl_or_b32 v84, v102, 6, v100
	v_mov_b32_e32 v85, v91
	global_store_dwordx4 v[74:75], v[76:79], off sc1
	v_lshl_add_u64 v[74:75], s[0:1], 0, v[60:61]
	v_pk_add_f32 v[50:51], v[10:11], v[50:51]
	v_pk_add_f32 v[48:49], v[8:9], v[48:49]
	v_pk_add_f32 v[42:43], v[6:7], v[42:43]
	v_pk_add_f32 v[40:41], v[4:5], v[40:41]
	v_pk_add_f32 v[62:63], v[6:7], v[62:63]
	v_cvt_pk_f16_f32 v48, v48, v49
	v_cvt_pk_f16_f32 v49, v50, v51
	v_cvt_pk_f16_f32 v50, v40, v41
	v_cvt_pk_f16_f32 v51, v42, v43
	v_lshl_add_u64 v[40:41], v[74:75], 0, v[84:85]
	v_cvt_pk_f16_f32 v71, v62, v63
	v_lshl_add_u64 v[60:61], v[74:75], 0, v[90:91]
	global_store_dwordx4 v[40:41], v[48:51], off sc1
	v_pk_add_f32 v[42:43], v[22:23], v[54:55]
	v_pk_add_f32 v[40:41], v[20:21], v[52:53]
	v_lshl_or_b32 v80, v103, 6, v100
	v_lshl_or_b32 v82, v104, 6, v100
	v_mov_b32_e32 v81, v91
	v_mov_b32_e32 v83, v91
	global_store_dwordx4 v[60:61], v[68:71], off sc1
	v_pk_add_f32 v[62:63], v[22:23], v[66:67]
	v_pk_add_f32 v[60:61], v[20:21], v[64:65]
	v_pk_add_f32 v[58:59], v[14:15], v[58:59]
	v_pk_add_f32 v[56:57], v[12:13], v[56:57]
	v_cvt_pk_f16_f32 v40, v40, v41
	v_cvt_pk_f16_f32 v41, v42, v43
	v_pk_add_f32 v[46:47], v[14:15], v[46:47]
	v_pk_add_f32 v[42:43], v[12:13], v[44:45]
	v_pk_add_f32 v[34:35], v[10:11], v[34:35]
	v_pk_add_f32 v[32:33], v[8:9], v[32:33]
	v_pk_add_f32 v[26:27], v[6:7], v[26:27]
	v_pk_add_f32 v[24:25], v[4:5], v[24:25]
	v_pk_add_f32 v[22:23], v[22:23], v[38:39]
	v_pk_add_f32 v[20:21], v[20:21], v[36:37]
	v_pk_add_f32 v[14:15], v[14:15], v[30:31]
	v_pk_add_f32 v[12:13], v[12:13], v[28:29]
	v_pk_add_f32 v[10:11], v[10:11], v[18:19]
	v_pk_add_f32 v[8:9], v[8:9], v[16:17]
	v_pk_add_f32 v[2:3], v[6:7], v[2:3]
	v_pk_add_f32 v[0:1], v[4:5], v[0:1]
	v_cvt_pk_f16_f32 v60, v60, v61
	v_cvt_pk_f16_f32 v61, v62, v63
	v_cvt_pk_f16_f32 v62, v56, v57
	v_cvt_pk_f16_f32 v63, v58, v59
	v_lshl_add_u64 v[56:57], v[72:73], 0, v[84:85]
	v_cvt_pk_f16_f32 v42, v42, v43
	v_cvt_pk_f16_f32 v43, v46, v47
	v_lshl_add_u64 v[44:45], v[72:73], 0, v[80:81]
	v_cvt_pk_f16_f32 v32, v32, v33
	v_cvt_pk_f16_f32 v33, v34, v35
	v_cvt_pk_f16_f32 v34, v24, v25
	v_cvt_pk_f16_f32 v35, v26, v27
	v_lshl_add_u64 v[24:25], v[74:75], 0, v[80:81]
	v_cvt_pk_f16_f32 v20, v20, v21
	v_cvt_pk_f16_f32 v21, v22, v23
	v_cvt_pk_f16_f32 v22, v12, v13
	v_cvt_pk_f16_f32 v23, v14, v15
	v_lshl_add_u64 v[12:13], v[72:73], 0, v[82:83]
	v_cvt_pk_f16_f32 v8, v8, v9
	v_cvt_pk_f16_f32 v9, v10, v11
	v_cvt_pk_f16_f32 v10, v0, v1
	v_cvt_pk_f16_f32 v11, v2, v3
	v_lshl_add_u64 v[0:1], v[74:75], 0, v[82:83]
	global_store_dwordx4 v[56:57], v[60:63], off sc1
	global_store_dwordx4 v[44:45], v[40:43], off sc1
	global_store_dwordx4 v[24:25], v[32:35], off sc1
	global_store_dwordx4 v[12:13], v[20:23], off sc1
	global_store_dwordx4 v[0:1], v[8:11], off sc1
	s_waitcnt vmcnt(0)
	s_cmpk_gt_u32 s18, 0xff
	s_cbranch_scc1 .LBB1_10
	s_barrier

.LBB2_3:
	s_mov_b32 s16, s15
	v_add_u32_e32 v116, s16, v87
	v_add_u32_e32 v148, s16, v0
	ds_read_b128 v[88:91], v116 offset:16384
	ds_read_b128 v[92:95], v116 offset:17408
	ds_read_b128 v[96:99], v116 offset:18432
	ds_read_b128 v[100:103], v116 offset:19456
	ds_read_b128 v[104:107], v116 offset:32768
	ds_read_b128 v[108:111], v116 offset:33792
	ds_read_b128 v[112:115], v116 offset:34816
	ds_read_b128 v[116:119], v116 offset:35840
	s_lshl_b32 s15, s7, 7
	s_ashr_i32 s17, s15, 31
	s_add_u32 s18, s4, s15
	s_addc_u32 s19, s5, s17
	s_add_u32 s20, s2, s15
	s_addc_u32 s21, s3, s17
	s_add_i32 s15, s6, s14
	s_add_i32 m0, s15, 0x4000
	s_nop 0
	global_load_lds_dwordx4 v82, s[18:19]
	ds_read_b128 v[120:123], v148
	ds_read_b128 v[124:127], v148 offset:1024
	ds_read_b128 v[128:131], v148 offset:2048
	s_add_i32 m0, s15, 0x6000
	s_nop 0
	global_load_lds_dwordx4 v84, s[18:19]
	ds_read_b128 v[132:135], v148 offset:3072
	ds_read_b128 v[136:139], v148 offset:4096
	ds_read_b128 v[140:143], v148 offset:5120
	s_mov_b32 m0, s15
	s_nop 0
	global_load_lds_dwordx4 v82, s[20:21]
	ds_read_b128 v[144:147], v148 offset:6144
	ds_read_b128 v[148:151], v148 offset:7168
	s_waitcnt vmcnt(3)
	s_waitcnt lgkmcnt(0)
	s_barrier
	s_setprio 1
	s_waitcnt lgkmcnt(0)
	v_mfma_f32_16x16x32_f16 v[18:21], v[88:91], v[120:123], v[18:21]
	s_add_u32 s18, s18, 0x40000
	s_addc_u32 s19, s19, 0
	s_add_i32 m0, s15, 0x8000
	v_mfma_f32_16x16x32_f16 v[70:73], v[96:99], v[120:123], v[70:73]
	global_load_lds_dwordx4 v82, s[18:19]
	v_mfma_f32_16x16x32_f16 v[58:61], v[88:91], v[128:131], v[58:61]
	s_add_i32 m0, s15, 0xa000
	v_mfma_f32_16x16x32_f16 v[54:57], v[96:99], v[128:131], v[54:57]
	global_load_lds_dwordx4 v84, s[18:19]
	v_mfma_f32_16x16x32_f16 v[18:21], v[92:95], v[124:127], v[18:21]
	s_add_i32 m0, s15, 0x2000
	v_mfma_f32_16x16x32_f16 v[70:73], v[100:103], v[124:127], v[70:73]
	global_load_lds_dwordx4 v84, s[20:21]
	v_mfma_f32_16x16x32_f16 v[58:61], v[92:95], v[132:135], v[58:61]
	v_mfma_f32_16x16x32_f16 v[54:57], v[100:103], v[132:135], v[54:57]
	v_mfma_f32_16x16x32_f16 v[42:45], v[88:91], v[136:139], v[42:45]
	v_mfma_f32_16x16x32_f16 v[38:41], v[96:99], v[136:139], v[38:41]
	v_mfma_f32_16x16x32_f16 v[26:29], v[88:91], v[144:147], v[26:29]
	v_mfma_f32_16x16x32_f16 v[22:25], v[96:99], v[144:147], v[22:25]
	v_mfma_f32_16x16x32_f16 v[42:45], v[92:95], v[140:143], v[42:45]
	v_mfma_f32_16x16x32_f16 v[38:41], v[100:103], v[140:143], v[38:41]
	v_mfma_f32_16x16x32_f16 v[26:29], v[92:95], v[148:151], v[26:29]
	v_mfma_f32_16x16x32_f16 v[22:25], v[100:103], v[148:151], v[22:25]
	v_mfma_f32_16x16x32_f16 v[78:81], v[104:107], v[120:123], v[78:81]
	v_mfma_f32_16x16x32_f16 v[74:77], v[112:115], v[120:123], v[74:77]
	v_mfma_f32_16x16x32_f16 v[66:69], v[104:107], v[128:131], v[66:69]
	v_mfma_f32_16x16x32_f16 v[62:65], v[112:115], v[128:131], v[62:65]
	v_mfma_f32_16x16x32_f16 v[78:81], v[108:111], v[124:127], v[78:81]
	v_mfma_f32_16x16x32_f16 v[74:77], v[116:119], v[124:127], v[74:77]
	v_mfma_f32_16x16x32_f16 v[66:69], v[108:111], v[132:135], v[66:69]
	v_mfma_f32_16x16x32_f16 v[62:65], v[116:119], v[132:135], v[62:65]
	v_mfma_f32_16x16x32_f16 v[50:53], v[104:107], v[136:139], v[50:53]
	v_mfma_f32_16x16x32_f16 v[46:49], v[112:115], v[136:139], v[46:49]
	s_add_i32 s7, s7, 1
	s_cmp_lg_u32 s7, 16
	v_mfma_f32_16x16x32_f16 v[34:37], v[104:107], v[144:147], v[34:37]
	s_cselect_b32 s7, s7, 0
	v_mfma_f32_16x16x32_f16 v[30:33], v[112:115], v[144:147], v[30:33]
	s_add_i32 s11, s11, -1
	v_mfma_f32_16x16x32_f16 v[50:53], v[108:111], v[140:143], v[50:53]
	s_mov_b32 s15, s13
	v_mfma_f32_16x16x32_f16 v[46:49], v[116:119], v[140:143], v[46:49]
	s_mov_b32 s13, s14
	v_mfma_f32_16x16x32_f16 v[34:37], v[108:111], v[148:151], v[34:37]
	s_mov_b32 s14, s16
	v_mfma_f32_16x16x32_f16 v[30:33], v[116:119], v[148:151], v[30:33]
	s_cmp_lg_u32 s11, 0
	s_setprio 0
	s_barrier
	s_cbranch_scc1 .LBB2_3
	v_lshl_add_u32 v0, s0, 7, v86
	v_or_b32_e32 v88, s10, v1
	v_ashrrev_i32_e32 v1, 31, v0
	v_lshlrev_b64 v[82:83], 12, v[0:1]
	v_or_b32_e32 v88, s1, v88
	v_lshl_add_u64 v[82:83], s[8:9], 0, v[82:83]
	v_lshlrev_b32_e32 v88, 2, v88
	v_mov_b32_e32 v89, 0
	v_or_b32_e32 v84, 16, v0
	v_lshl_add_u64 v[82:83], v[82:83], 0, v[88:89]
	v_pk_add_f32 v[20:21], v[16:17], v[20:21]
	v_pk_add_f32 v[18:19], v[14:15], v[18:19]
	v_ashrrev_i32_e32 v85, 31, v84
	global_store_dwordx4 v[82:83], v[18:21], off sc1
	v_lshlrev_b64 v[84:85], 12, v[84:85]
	v_lshl_add_u64 v[84:85], s[8:9], 0, v[84:85]
	v_pk_add_f32 v[20:21], v[12:13], v[72:73]
	v_pk_add_f32 v[18:19], v[10:11], v[70:71]
	global_store_dwordx4 v[82:83], v[18:21], off offset:64 sc1
	v_or_b32_e32 v86, 32, v0
	v_lshl_add_u64 v[84:85], v[84:85], 0, v[88:89]
	v_pk_add_f32 v[20:21], v[8:9], v[80:81]
	v_pk_add_f32 v[18:19], v[6:7], v[78:79]
	global_store_dwordx4 v[82:83], v[18:21], off offset:512 sc1
	v_ashrrev_i32_e32 v87, 31, v86
	v_lshlrev_b64 v[86:87], 12, v[86:87]
	v_pk_add_f32 v[20:21], v[4:5], v[76:77]
	v_pk_add_f32 v[18:19], v[2:3], v[74:75]
	global_store_dwordx4 v[82:83], v[18:21], off offset:576 sc1
	v_lshl_add_u64 v[86:87], s[8:9], 0, v[86:87]
	v_or_b32_e32 v0, 48, v0
	v_pk_add_f32 v[20:21], v[16:17], v[60:61]
	v_pk_add_f32 v[18:19], v[14:15], v[58:59]
	global_store_dwordx4 v[84:85], v[18:21], off sc1
	v_ashrrev_i32_e32 v1, 31, v0
	v_lshl_add_u64 v[86:87], v[86:87], 0, v[88:89]
	v_pk_add_f32 v[20:21], v[12:13], v[56:57]
	v_pk_add_f32 v[18:19], v[10:11], v[54:55]
	global_store_dwordx4 v[84:85], v[18:21], off offset:64 sc1
	v_lshlrev_b64 v[0:1], 12, v[0:1]
	v_lshl_add_u64 v[0:1], s[8:9], 0, v[0:1]
	v_pk_add_f32 v[20:21], v[8:9], v[68:69]
	v_pk_add_f32 v[18:19], v[6:7], v[66:67]
	global_store_dwordx4 v[84:85], v[18:21], off offset:512 sc1
	v_lshl_add_u64 v[0:1], v[0:1], 0, v[88:89]
	s_cmpk_gt_u32 s12, 0xff
	v_pk_add_f32 v[20:21], v[4:5], v[64:65]
	v_pk_add_f32 v[18:19], v[2:3], v[62:63]
	global_store_dwordx4 v[84:85], v[18:21], off offset:576 sc1
	s_nop 1
	v_pk_add_f32 v[20:21], v[16:17], v[44:45]
	v_pk_add_f32 v[18:19], v[14:15], v[42:43]
	global_store_dwordx4 v[86:87], v[18:21], off sc1
	v_pk_add_f32 v[16:17], v[16:17], v[28:29]
	v_pk_add_f32 v[14:15], v[14:15], v[26:27]
	v_pk_add_f32 v[20:21], v[12:13], v[40:41]
	v_pk_add_f32 v[18:19], v[10:11], v[38:39]
	global_store_dwordx4 v[86:87], v[18:21], off offset:64 sc1
	v_pk_add_f32 v[12:13], v[12:13], v[24:25]
	v_pk_add_f32 v[10:11], v[10:11], v[22:23]
	v_pk_add_f32 v[20:21], v[8:9], v[52:53]
	v_pk_add_f32 v[18:19], v[6:7], v[50:51]
	global_store_dwordx4 v[86:87], v[18:21], off offset:512 sc1
	v_pk_add_f32 v[8:9], v[8:9], v[36:37]
	v_pk_add_f32 v[6:7], v[6:7], v[34:35]
	v_pk_add_f32 v[20:21], v[4:5], v[48:49]
	v_pk_add_f32 v[18:19], v[2:3], v[46:47]
	v_pk_add_f32 v[4:5], v[4:5], v[32:33]
	v_pk_add_f32 v[2:3], v[2:3], v[30:31]
	global_store_dwordx4 v[86:87], v[18:21], off offset:576 sc1
	global_store_dwordx4 v[0:1], v[14:17], off sc1
	global_store_dwordx4 v[0:1], v[10:13], off offset:64 sc1
	global_store_dwordx4 v[0:1], v[6:9], off offset:512 sc1
	global_store_dwordx4 v[0:1], v[2:5], off offset:576 sc1
	s_waitcnt vmcnt(0)
	s_cbranch_scc1 .LBB2_6
	s_barrier
